# attention loop: no static priority for waves 4-7 inside the hand-written loop
# baseline (speedup 1.0000x reference)
; #define AT_LOADK(t) do { const int kr_ = AT_KROW(t); _Pragma("unroll") for (int i_ = 0; i_ < 2; ++i_) kreg[i_] = *(const u32x4*)(Kp + (size_t)(kr_ + prow0 + 32 * i_) * 512 + pch * 8); } while (0)
; #define AT_LOADV(t) do { const int kr_ = AT_KROW(t); _Pragma("unroll") for (int i_ = 0; i_ < 2; ++i_) vreg[i_] = *(const u32x4*)(Vp + (size_t)(kr_ + prow0 + 32 * i_) * 512 + pch * 8); } while (0)
; #define AT_STOREK(st) do { _Pragma("unroll") for (int i_ = 0; i_ < 2; ++i_) *(LAS u32x4*)(L + AT_K + (st) * AT_KBYTES + (prow0 + 32 * i_) * AT_KSTR + pch * 16) = kreg[i_]; } while (0)
; #define AT_STOREV(st) do { _Pragma("unroll") for (int i_ = 0; i_ < 2; ++i_) *(LAS u32x4*)(L + AT_V + (st) * AT_VBYTES + (prow0 + 32 * i_) * AT_VSTR + pch * 16) = vreg[i_]; } while (0)
; __device__ __forceinline__ void attn_unit(const Frame& F, int layer, int qrow0, int ntiles, int b, int head, float lam, float m2, float lam_init) {
;     ...
;     if (wave >= 4) __builtin_amdgcn_s_setprio(1);
;     AT_LOADK(0); AT_LOADV(0); AT_STOREK(0); AT_STOREV(0);
;     if (ntiles > 1) { AT_LOADK(1); AT_STOREK(1); }
;     __syncthreads();
.LBB0_549:
	s_add_u32 s42, s4, s30
	s_addc_u32 s43, s5, 0
	s_add_u32 s2, s2, s30
	s_addc_u32 s3, s3, 0
	s_lshl_b32 s4, s16, 8
	v_ashrrev_i32_e32 v186, 4, v32
	s_add_i32 s5, s4, 0x8000
	s_add_i32 s16, s4, 0x8040
	v_lshlrev_b32_e32 v3, 4, v32
	v_add_u32_e32 v128, s5, v186
	v_and_b32_e32 v144, 0xf0, v3
	v_add_u32_e32 v20, s16, v186
	v_lshl_add_u64 v[4:5], s[2:3], 0, v[144:145]
	s_mov_b64 s[2:3], 0x31534800
	v_ashrrev_i32_e32 v129, 31, v128
	v_ashrrev_i32_e32 v21, 31, v20
	v_lshl_add_u64 v[180:181], v[4:5], 0, s[2:3]
	v_lshlrev_b64 v[12:13], 10, v[128:129]
	s_mov_b64 s[2:3], 0x8000
	v_lshl_add_u64 v[16:17], s[42:43], 0, v[144:145]
	s_mov_b64 s[42:43], 0x33934800
	v_lshlrev_b64 v[62:63], 10, v[20:21]
	v_lshl_add_u64 v[14:15], v[12:13], 0, s[2:3]
	v_lshl_add_u64 v[182:183], v[16:17], 0, s[42:43]
	v_lshl_add_u64 v[96:97], v[62:63], 0, s[2:3]
	v_lshl_add_u64 v[4:5], v[180:181], 0, v[12:13]
	v_lshl_add_u64 v[8:9], v[180:181], 0, v[14:15]
	v_lshl_add_u64 v[12:13], v[182:183], 0, v[12:13]
	v_lshl_add_u64 v[16:17], v[182:183], 0, v[14:15]
	v_lshl_add_u64 v[20:21], v[180:181], 0, v[62:63]
	v_lshl_add_u64 v[24:25], v[180:181], 0, v[96:97]
	global_load_dwordx4 v[4:7], v[4:5], off
	s_nop 0
	global_load_dwordx4 v[8:11], v[8:9], off
	s_nop 0
	global_load_dwordx4 v[12:15], v[12:13], off
	s_nop 0
	global_load_dwordx4 v[16:19], v[16:17], off
	s_nop 0
	global_load_dwordx4 v[20:23], v[20:21], off
	s_nop 0
	global_load_dwordx4 v[24:27], v[24:25], off
	v_or_b32_e32 v1, s15, v1
	s_movk_i32 s16, 0x140
	v_mul_u32_u24_e32 v0, 0x110, v0
	v_mul_lo_u32 v198, v186, s24
	v_mul_lo_u32 v199, v186, s16
	v_lshlrev_b32_e32 v1, 1, v1
	v_add_u32_e32 v200, 0, v144
	v_xor_b32_e32 v64, 0x80000000, v2
	v_add_u32_e32 v2, 0x2800, v199
	v_add3_u32 v197, 0, v0, v1
	v_add_u32_e32 v144, v200, v198
	v_add_u32_e32 v194, v200, v199
	v_add_u32_e32 v195, v200, v2
	v_mov_b32_e32 v65, v64
	v_mov_b32_e32 v66, v64
	v_mov_b32_e32 v67, v64
	v_mov_b32_e32 v68, v64
	v_mov_b32_e32 v69, v64
	v_mov_b32_e32 v70, v64
	v_mov_b32_e32 v71, v64
	v_mov_b32_e32 v72, v64
	v_mov_b32_e32 v73, v64
	v_mov_b32_e32 v74, v64
	v_mov_b32_e32 v75, v64
	v_mov_b32_e32 v76, v64
	v_mov_b32_e32 v77, v64
	v_mov_b32_e32 v78, v64
	v_mov_b32_e32 v79, v64
	v_and_b32_e32 v193, 63, v32
	v_and_b32_e32 v33, 16, v32
	s_mov_b32 s15, 0x8000
	s_mov_b32 s2, 4
	s_mov_b32 s3, 0
	s_add_i32 s5, s4, 0x8080
	s_add_i32 s4, s4, 0x80c0
	s_waitcnt vmcnt(5)
	ds_write_b128 v144, v[4:7]
	s_waitcnt vmcnt(4)
	ds_write_b128 v144, v[8:11] offset:8704
	s_waitcnt vmcnt(3)
	ds_write_b128 v194, v[12:15] offset:34816
	s_waitcnt vmcnt(2)
	ds_write_b128 v195, v[16:19] offset:34816
	s_waitcnt vmcnt(1)
	ds_write_b128 v144, v[20:23] offset:17408
	s_waitcnt vmcnt(0)
	ds_write_b128 v144, v[24:27] offset:26112
	s_waitcnt lgkmcnt(0)
	s_barrier
	s_setprio 0
	v_readfirstlane_b32 s72, v180
	v_readfirstlane_b32 s73, v181
	v_readfirstlane_b32 s74, v182
	v_readfirstlane_b32 s75, v183
	v_lshl_add_u32 v178, v186, 10, v200
	v_mov_b32_e32 v252, v64
	s_add_i32 s42, s4, 0xffffff40
	s_add_i32 s43, s4, 0xffff7f40
	s_lshl_b32 s43, s43, 3
	s_add_i32 s43, s43, 0xffffff00
	s_mov_b32 s2, 0
	s_add_i32 s5, s2, 2
	s_cmp_ge_u32 s5, 36
	s_cbranch_scc1 .Latt_nokload_pro1
	s_cmp_lt_u32 s5, 4
	s_cselect_b32 s15, s42, s43
	s_lshl_b32 s45, s5, 6
	s_add_i32 s15, s15, s45
	s_lshl_b32 s15, s15, 10
	v_add_u32_e32 v186, s15, v178
	v_add_u32_e32 v187, 0x8000, v186
	global_load_dwordx4 v[162:165], v186, s[72:73]
	global_load_dwordx4 v[166:169], v187, s[72:73]
